# chunk-state scan rewritten by hand: straight-line 32 steps, loads of step n+10 issued at step n into a ring of free registers, counted vmcnt waits (both layers)
# baseline (speedup 1.0000x reference)
; #define GAS __attribute__((address_space(1)))
; __device__ __forceinline__ unsigned cvt_pk_bf16(float lo, float hi) { unsigned r; asm volatile("v_cvt_pk_bf16_f32 %0, %1, %2" : "=v"(r) : "v"(lo), "v"(hi)); return r; }
; #define PHASE_IDS() int tid = threadIdx.x; asm volatile("" : "+v"(tid)); const int lane = tid & 63, w = __builtin_amdgcn_readfirstlane(tid >> 6); (void)lane; (void)w
; __device__ __forceinline__ void scan_item(Frame& F, int item) {
;     const GAS float* UT = (const GAS float*)(F.ws + WS_UT); const GAS float* DEC = (const GAS float*)(F.ws + WS_DEC); GAS bf16_t* SPT = (GAS bf16_t*)(F.ws + WS_SPT);
;     PHASE_IDS();
;     const int bh = item >> 2, q4 = item & 3, vv = q4 * 32 + (tid >> 4), kk0 = (tid & 15) * 8;
;     f32x4 s0 = {0.f, 0.f, 0.f, 0.f}, s1 = {0.f, 0.f, 0.f, 0.f};
; #pragma unroll 16
;     for (int n = 0; n < 32; ++n) { const size_t chunk = (size_t)bh * 32 + n; const size_t eo = chunk * 16384 + (size_t)vv * 128 + kk0;
;         const u32x4 ub = *(const GAS u32x4*)((const GAS bf16_t*)UT + eo); const f32x4 u0 = {bflo(ub.x), bfhi(ub.x), bflo(ub.y), bfhi(ub.y)}, u1 = {bflo(ub.z), bfhi(ub.z), bflo(ub.w), bfhi(ub.w)}, d0 = *(const GAS f32x4*)(DEC + chunk * 128 + kk0), d1 = *(const GAS f32x4*)(DEC + chunk * 128 + kk0 + 4);
;         u32x4 wv; wv.x = cvt_pk_bf16(s0[0], s0[1]); wv.y = cvt_pk_bf16(s0[2], s0[3]); wv.z = cvt_pk_bf16(s1[0], s1[1]); wv.w = cvt_pk_bf16(s1[2], s1[3]);
;         *(GAS u32x4*)(SPT + eo) = wv;
;         s0 = d0 * s0 + u0; s1 = d1 * s1 + u1; }
; }
.LBB0_887:
	s_waitcnt vmcnt(0)
	s_ashr_i32 s4, s85, 2
	s_and_b32 s5, s85, 3
	s_lshl_b32 s86, s4, 20
	s_lshl_b32 s87, s5, 13
	s_or_b32 s86, s86, s87
	s_add_u32 s88, s52, 0x5cb00000
	s_addc_u32 s89, s53, 0
	s_add_u32 s88, s88, s86
	s_addc_u32 s89, s89, 0
	v_lshrrev_b32_e32 v2, 4, v0
	v_lshlrev_b32_e32 v2, 8, v2
	v_and_b32_e32 v8, 15, v0
	v_lshl_or_b32 v2, v8, 4, v2
	v_mov_b32_e32 v3, 0
	v_lshl_add_u64 v[4:5], s[88:89], 0, v[2:3]
	s_mov_b64 s[86:87], 0x8000000
	v_lshl_add_u64 v[6:7], v[4:5], 0, s[86:87]
	s_lshl_b32 s86, s4, 14
	s_add_u32 s88, s52, 0x68b00000
	s_addc_u32 s89, s53, 0
	s_add_u32 s88, s88, s86
	s_addc_u32 s89, s89, 0
	v_lshlrev_b32_e32 v8, 5, v8
	v_mov_b32_e32 v9, 0
	v_lshl_add_u64 v[10:11], s[88:89], 0, v[8:9]
	s_mov_b64 s[4:5], 0x8000
	s_mov_b64 s[86:87], 0x1000
	v_mov_b32_e32 v12, 0
	v_mov_b32_e32 v13, 0
	v_mov_b32_e32 v14, 0
	v_mov_b32_e32 v15, 0
	v_mov_b32_e32 v16, 0
	v_mov_b32_e32 v17, 0
	v_mov_b32_e32 v18, 0
	v_mov_b32_e32 v19, 0
	global_load_dwordx4 v[118:121], v[4:5], off
	v_lshl_add_u64 v[4:5], v[4:5], 0, s[4:5]
	global_load_dwordx4 v[122:125], v[10:11], off offset:0
	global_load_dwordx4 v[126:129], v[10:11], off offset:16
	global_load_dwordx4 v[130:133], v[4:5], off
	v_lshl_add_u64 v[4:5], v[4:5], 0, s[4:5]
	global_load_dwordx4 v[134:137], v[10:11], off offset:512
	global_load_dwordx4 v[138:141], v[10:11], off offset:528
	global_load_dwordx4 v[142:145], v[4:5], off
	v_lshl_add_u64 v[4:5], v[4:5], 0, s[4:5]
	global_load_dwordx4 v[146:149], v[10:11], off offset:1024
	global_load_dwordx4 v[150:153], v[10:11], off offset:1040
	global_load_dwordx4 v[154:157], v[4:5], off
	v_lshl_add_u64 v[4:5], v[4:5], 0, s[4:5]
	global_load_dwordx4 v[158:161], v[10:11], off offset:1536
	global_load_dwordx4 v[162:165], v[10:11], off offset:1552
	global_load_dwordx4 v[166:169], v[4:5], off
	v_lshl_add_u64 v[4:5], v[4:5], 0, s[4:5]
	global_load_dwordx4 v[170:173], v[10:11], off offset:2048
	global_load_dwordx4 v[174:177], v[10:11], off offset:2064
	global_load_dwordx4 v[178:181], v[4:5], off
	v_lshl_add_u64 v[4:5], v[4:5], 0, s[4:5]
	global_load_dwordx4 v[182:185], v[10:11], off offset:2560
	global_load_dwordx4 v[186:189], v[10:11], off offset:2576
	global_load_dwordx4 v[190:193], v[4:5], off
	v_lshl_add_u64 v[4:5], v[4:5], 0, s[4:5]
	global_load_dwordx4 v[194:197], v[10:11], off offset:3072
	global_load_dwordx4 v[198:201], v[10:11], off offset:3088
	global_load_dwordx4 v[202:205], v[4:5], off
	v_lshl_add_u64 v[4:5], v[4:5], 0, s[4:5]
	global_load_dwordx4 v[206:209], v[10:11], off offset:3584
	global_load_dwordx4 v[210:213], v[10:11], off offset:3600
	v_lshl_add_u64 v[10:11], v[10:11], 0, s[86:87]
	global_load_dwordx4 v[214:217], v[4:5], off
	v_lshl_add_u64 v[4:5], v[4:5], 0, s[4:5]
	global_load_dwordx4 v[218:221], v[10:11], off offset:0
	global_load_dwordx4 v[222:225], v[10:11], off offset:16
	global_load_dwordx4 v[226:229], v[4:5], off
	v_lshl_add_u64 v[4:5], v[4:5], 0, s[4:5]
	global_load_dwordx4 v[230:233], v[10:11], off offset:512
	global_load_dwordx4 v[234:237], v[10:11], off offset:528
	s_waitcnt vmcnt(27)
	v_cvt_pk_bf16_f32 v28, v12, v13
	v_cvt_pk_bf16_f32 v29, v14, v15
	v_cvt_pk_bf16_f32 v30, v16, v17
	v_cvt_pk_bf16_f32 v31, v18, v19
	global_store_dwordx4 v[6:7], v[28:31], off
	v_lshl_add_u64 v[6:7], v[6:7], 0, s[4:5]
	v_lshlrev_b32_e32 v20, 16, v118
	v_and_b32_e32 v21, 0xffff0000, v118
	v_lshlrev_b32_e32 v22, 16, v119
	v_and_b32_e32 v23, 0xffff0000, v119
	v_lshlrev_b32_e32 v24, 16, v120
	v_and_b32_e32 v25, 0xffff0000, v120
	v_lshlrev_b32_e32 v26, 16, v121
	v_and_b32_e32 v27, 0xffff0000, v121
	v_pk_fma_f32 v[12:13], v[12:13], v[122:123], v[20:21]
	v_pk_fma_f32 v[14:15], v[14:15], v[124:125], v[22:23]
	v_pk_fma_f32 v[16:17], v[16:17], v[126:127], v[24:25]
	v_pk_fma_f32 v[18:19], v[18:19], v[128:129], v[26:27]
	global_load_dwordx4 v[118:121], v[4:5], off
	v_lshl_add_u64 v[4:5], v[4:5], 0, s[4:5]
	global_load_dwordx4 v[122:125], v[10:11], off offset:1024
	global_load_dwordx4 v[126:129], v[10:11], off offset:1040
	s_waitcnt vmcnt(28)
	v_cvt_pk_bf16_f32 v28, v12, v13
	v_cvt_pk_bf16_f32 v29, v14, v15
	v_cvt_pk_bf16_f32 v30, v16, v17
	v_cvt_pk_bf16_f32 v31, v18, v19
	global_store_dwordx4 v[6:7], v[28:31], off
	v_lshl_add_u64 v[6:7], v[6:7], 0, s[4:5]
	v_lshlrev_b32_e32 v20, 16, v130
	v_and_b32_e32 v21, 0xffff0000, v130
	v_lshlrev_b32_e32 v22, 16, v131
	v_and_b32_e32 v23, 0xffff0000, v131
	v_lshlrev_b32_e32 v24, 16, v132
	v_and_b32_e32 v25, 0xffff0000, v132
	v_lshlrev_b32_e32 v26, 16, v133
	v_and_b32_e32 v27, 0xffff0000, v133
	v_pk_fma_f32 v[12:13], v[12:13], v[134:135], v[20:21]
	v_pk_fma_f32 v[14:15], v[14:15], v[136:137], v[22:23]
	v_pk_fma_f32 v[16:17], v[16:17], v[138:139], v[24:25]
	v_pk_fma_f32 v[18:19], v[18:19], v[140:141], v[26:27]
	global_load_dwordx4 v[130:133], v[4:5], off
	v_lshl_add_u64 v[4:5], v[4:5], 0, s[4:5]
	global_load_dwordx4 v[134:137], v[10:11], off offset:1536
	global_load_dwordx4 v[138:141], v[10:11], off offset:1552
	s_waitcnt vmcnt(29)
	v_cvt_pk_bf16_f32 v28, v12, v13
	v_cvt_pk_bf16_f32 v29, v14, v15
	v_cvt_pk_bf16_f32 v30, v16, v17
	v_cvt_pk_bf16_f32 v31, v18, v19
	global_store_dwordx4 v[6:7], v[28:31], off
	v_lshl_add_u64 v[6:7], v[6:7], 0, s[4:5]
	v_lshlrev_b32_e32 v20, 16, v142
	v_and_b32_e32 v21, 0xffff0000, v142
	v_lshlrev_b32_e32 v22, 16, v143
	v_and_b32_e32 v23, 0xffff0000, v143
	v_lshlrev_b32_e32 v24, 16, v144
	v_and_b32_e32 v25, 0xffff0000, v144
	v_lshlrev_b32_e32 v26, 16, v145
	v_and_b32_e32 v27, 0xffff0000, v145
	v_pk_fma_f32 v[12:13], v[12:13], v[146:147], v[20:21]
	v_pk_fma_f32 v[14:15], v[14:15], v[148:149], v[22:23]
	v_pk_fma_f32 v[16:17], v[16:17], v[150:151], v[24:25]
	v_pk_fma_f32 v[18:19], v[18:19], v[152:153], v[26:27]
	global_load_dwordx4 v[142:145], v[4:5], off
	v_lshl_add_u64 v[4:5], v[4:5], 0, s[4:5]
	global_load_dwordx4 v[146:149], v[10:11], off offset:2048
	global_load_dwordx4 v[150:153], v[10:11], off offset:2064
	s_waitcnt vmcnt(30)
; #define GAS __attribute__((address_space(1)))
; __device__ __forceinline__ unsigned cvt_pk_bf16(float lo, float hi) { unsigned r; asm volatile("v_cvt_pk_bf16_f32 %0, %1, %2" : "=v"(r) : "v"(lo), "v"(hi)); return r; }
; __device__ __forceinline__ void scan_item(Frame& F, int item) {
;     ...
; #pragma unroll 16
;     for (int n = 0; n < 32; ++n) { const size_t chunk = (size_t)bh * 32 + n; const size_t eo = chunk * 16384 + (size_t)vv * 128 + kk0;
;         const u32x4 ub = *(const GAS u32x4*)((const GAS bf16_t*)UT + eo); const f32x4 u0 = {bflo(ub.x), bfhi(ub.x), bflo(ub.y), bfhi(ub.y)}, u1 = {bflo(ub.z), bfhi(ub.z), bflo(ub.w), bfhi(ub.w)}, d0 = *(const GAS f32x4*)(DEC + chunk * 128 + kk0), d1 = *(const GAS f32x4*)(DEC + chunk * 128 + kk0 + 4);
;         u32x4 wv; wv.x = cvt_pk_bf16(s0[0], s0[1]); wv.y = cvt_pk_bf16(s0[2], s0[3]); wv.z = cvt_pk_bf16(s1[0], s1[1]); wv.w = cvt_pk_bf16(s1[2], s1[3]);
;         *(GAS u32x4*)(SPT + eo) = wv;
;         s0 = d0 * s0 + u0; s1 = d1 * s1 + u1; }
	v_cvt_pk_bf16_f32 v28, v12, v13
	v_cvt_pk_bf16_f32 v29, v14, v15
	v_cvt_pk_bf16_f32 v30, v16, v17
	v_cvt_pk_bf16_f32 v31, v18, v19
	global_store_dwordx4 v[6:7], v[28:31], off
	v_lshl_add_u64 v[6:7], v[6:7], 0, s[4:5]
	v_lshlrev_b32_e32 v20, 16, v154
	v_and_b32_e32 v21, 0xffff0000, v154
	v_lshlrev_b32_e32 v22, 16, v155
	v_and_b32_e32 v23, 0xffff0000, v155
	v_lshlrev_b32_e32 v24, 16, v156
	v_and_b32_e32 v25, 0xffff0000, v156
	v_lshlrev_b32_e32 v26, 16, v157
	v_and_b32_e32 v27, 0xffff0000, v157
	v_pk_fma_f32 v[12:13], v[12:13], v[158:159], v[20:21]
	v_pk_fma_f32 v[14:15], v[14:15], v[160:161], v[22:23]
	v_pk_fma_f32 v[16:17], v[16:17], v[162:163], v[24:25]
	v_pk_fma_f32 v[18:19], v[18:19], v[164:165], v[26:27]
	global_load_dwordx4 v[154:157], v[4:5], off
	v_lshl_add_u64 v[4:5], v[4:5], 0, s[4:5]
	global_load_dwordx4 v[158:161], v[10:11], off offset:2560
	global_load_dwordx4 v[162:165], v[10:11], off offset:2576
	s_waitcnt vmcnt(31)
	v_cvt_pk_bf16_f32 v28, v12, v13
	v_cvt_pk_bf16_f32 v29, v14, v15
	v_cvt_pk_bf16_f32 v30, v16, v17
	v_cvt_pk_bf16_f32 v31, v18, v19
	global_store_dwordx4 v[6:7], v[28:31], off
	v_lshl_add_u64 v[6:7], v[6:7], 0, s[4:5]
	v_lshlrev_b32_e32 v20, 16, v166
	v_and_b32_e32 v21, 0xffff0000, v166
	v_lshlrev_b32_e32 v22, 16, v167
	v_and_b32_e32 v23, 0xffff0000, v167
	v_lshlrev_b32_e32 v24, 16, v168
	v_and_b32_e32 v25, 0xffff0000, v168
	v_lshlrev_b32_e32 v26, 16, v169
	v_and_b32_e32 v27, 0xffff0000, v169
	v_pk_fma_f32 v[12:13], v[12:13], v[170:171], v[20:21]
	v_pk_fma_f32 v[14:15], v[14:15], v[172:173], v[22:23]
	v_pk_fma_f32 v[16:17], v[16:17], v[174:175], v[24:25]
	v_pk_fma_f32 v[18:19], v[18:19], v[176:177], v[26:27]
	global_load_dwordx4 v[166:169], v[4:5], off
	v_lshl_add_u64 v[4:5], v[4:5], 0, s[4:5]
	global_load_dwordx4 v[170:173], v[10:11], off offset:3072
	global_load_dwordx4 v[174:177], v[10:11], off offset:3088
	s_waitcnt vmcnt(32)
	v_cvt_pk_bf16_f32 v28, v12, v13
	v_cvt_pk_bf16_f32 v29, v14, v15
	v_cvt_pk_bf16_f32 v30, v16, v17
	v_cvt_pk_bf16_f32 v31, v18, v19
	global_store_dwordx4 v[6:7], v[28:31], off
	v_lshl_add_u64 v[6:7], v[6:7], 0, s[4:5]
	v_lshlrev_b32_e32 v20, 16, v178
	v_and_b32_e32 v21, 0xffff0000, v178
	v_lshlrev_b32_e32 v22, 16, v179
	v_and_b32_e32 v23, 0xffff0000, v179
	v_lshlrev_b32_e32 v24, 16, v180
	v_and_b32_e32 v25, 0xffff0000, v180
	v_lshlrev_b32_e32 v26, 16, v181
	v_and_b32_e32 v27, 0xffff0000, v181
	v_pk_fma_f32 v[12:13], v[12:13], v[182:183], v[20:21]
	v_pk_fma_f32 v[14:15], v[14:15], v[184:185], v[22:23]
	v_pk_fma_f32 v[16:17], v[16:17], v[186:187], v[24:25]
	v_pk_fma_f32 v[18:19], v[18:19], v[188:189], v[26:27]
	global_load_dwordx4 v[178:181], v[4:5], off
	v_lshl_add_u64 v[4:5], v[4:5], 0, s[4:5]
	global_load_dwordx4 v[182:185], v[10:11], off offset:3584
	global_load_dwordx4 v[186:189], v[10:11], off offset:3600
	v_lshl_add_u64 v[10:11], v[10:11], 0, s[86:87]
	s_waitcnt vmcnt(33)
	v_cvt_pk_bf16_f32 v28, v12, v13
	v_cvt_pk_bf16_f32 v29, v14, v15
	v_cvt_pk_bf16_f32 v30, v16, v17
	v_cvt_pk_bf16_f32 v31, v18, v19
	global_store_dwordx4 v[6:7], v[28:31], off
	v_lshl_add_u64 v[6:7], v[6:7], 0, s[4:5]
	v_lshlrev_b32_e32 v20, 16, v190
	v_and_b32_e32 v21, 0xffff0000, v190
	v_lshlrev_b32_e32 v22, 16, v191
	v_and_b32_e32 v23, 0xffff0000, v191
	v_lshlrev_b32_e32 v24, 16, v192
	v_and_b32_e32 v25, 0xffff0000, v192
	v_lshlrev_b32_e32 v26, 16, v193
	v_and_b32_e32 v27, 0xffff0000, v193
	v_pk_fma_f32 v[12:13], v[12:13], v[194:195], v[20:21]
	v_pk_fma_f32 v[14:15], v[14:15], v[196:197], v[22:23]
	v_pk_fma_f32 v[16:17], v[16:17], v[198:199], v[24:25]
	v_pk_fma_f32 v[18:19], v[18:19], v[200:201], v[26:27]
	global_load_dwordx4 v[190:193], v[4:5], off
	v_lshl_add_u64 v[4:5], v[4:5], 0, s[4:5]
	global_load_dwordx4 v[194:197], v[10:11], off offset:0
	global_load_dwordx4 v[198:201], v[10:11], off offset:16
	s_waitcnt vmcnt(34)
	v_cvt_pk_bf16_f32 v28, v12, v13
	v_cvt_pk_bf16_f32 v29, v14, v15
	v_cvt_pk_bf16_f32 v30, v16, v17
	v_cvt_pk_bf16_f32 v31, v18, v19
	global_store_dwordx4 v[6:7], v[28:31], off
	v_lshl_add_u64 v[6:7], v[6:7], 0, s[4:5]
	v_lshlrev_b32_e32 v20, 16, v202
	v_and_b32_e32 v21, 0xffff0000, v202
	v_lshlrev_b32_e32 v22, 16, v203
	v_and_b32_e32 v23, 0xffff0000, v203
	v_lshlrev_b32_e32 v24, 16, v204
	v_and_b32_e32 v25, 0xffff0000, v204
	v_lshlrev_b32_e32 v26, 16, v205
	v_and_b32_e32 v27, 0xffff0000, v205
	v_pk_fma_f32 v[12:13], v[12:13], v[206:207], v[20:21]
	v_pk_fma_f32 v[14:15], v[14:15], v[208:209], v[22:23]
	v_pk_fma_f32 v[16:17], v[16:17], v[210:211], v[24:25]
	v_pk_fma_f32 v[18:19], v[18:19], v[212:213], v[26:27]
	global_load_dwordx4 v[202:205], v[4:5], off
	v_lshl_add_u64 v[4:5], v[4:5], 0, s[4:5]
	global_load_dwordx4 v[206:209], v[10:11], off offset:512
	global_load_dwordx4 v[210:213], v[10:11], off offset:528
	s_waitcnt vmcnt(35)
	v_cvt_pk_bf16_f32 v28, v12, v13
	v_cvt_pk_bf16_f32 v29, v14, v15
	v_cvt_pk_bf16_f32 v30, v16, v17
	v_cvt_pk_bf16_f32 v31, v18, v19
	global_store_dwordx4 v[6:7], v[28:31], off
	v_lshl_add_u64 v[6:7], v[6:7], 0, s[4:5]
	v_lshlrev_b32_e32 v20, 16, v214
	v_and_b32_e32 v21, 0xffff0000, v214
	v_lshlrev_b32_e32 v22, 16, v215
	v_and_b32_e32 v23, 0xffff0000, v215
	v_lshlrev_b32_e32 v24, 16, v216
	v_and_b32_e32 v25, 0xffff0000, v216
	v_lshlrev_b32_e32 v26, 16, v217
	v_and_b32_e32 v27, 0xffff0000, v217
	v_pk_fma_f32 v[12:13], v[12:13], v[218:219], v[20:21]
	v_pk_fma_f32 v[14:15], v[14:15], v[220:221], v[22:23]
	v_pk_fma_f32 v[16:17], v[16:17], v[222:223], v[24:25]
	v_pk_fma_f32 v[18:19], v[18:19], v[224:225], v[26:27]
	global_load_dwordx4 v[214:217], v[4:5], off
	v_lshl_add_u64 v[4:5], v[4:5], 0, s[4:5]
	global_load_dwordx4 v[218:221], v[10:11], off offset:1024
	global_load_dwordx4 v[222:225], v[10:11], off offset:1040
	s_waitcnt vmcnt(36)
; #define GAS __attribute__((address_space(1)))
; __device__ __forceinline__ unsigned cvt_pk_bf16(float lo, float hi) { unsigned r; asm volatile("v_cvt_pk_bf16_f32 %0, %1, %2" : "=v"(r) : "v"(lo), "v"(hi)); return r; }
; __device__ __forceinline__ void scan_item(Frame& F, int item) {
;     ...
; #pragma unroll 16
;     for (int n = 0; n < 32; ++n) { const size_t chunk = (size_t)bh * 32 + n; const size_t eo = chunk * 16384 + (size_t)vv * 128 + kk0;
;         const u32x4 ub = *(const GAS u32x4*)((const GAS bf16_t*)UT + eo); const f32x4 u0 = {bflo(ub.x), bfhi(ub.x), bflo(ub.y), bfhi(ub.y)}, u1 = {bflo(ub.z), bfhi(ub.z), bflo(ub.w), bfhi(ub.w)}, d0 = *(const GAS f32x4*)(DEC + chunk * 128 + kk0), d1 = *(const GAS f32x4*)(DEC + chunk * 128 + kk0 + 4);
;         u32x4 wv; wv.x = cvt_pk_bf16(s0[0], s0[1]); wv.y = cvt_pk_bf16(s0[2], s0[3]); wv.z = cvt_pk_bf16(s1[0], s1[1]); wv.w = cvt_pk_bf16(s1[2], s1[3]);
;         *(GAS u32x4*)(SPT + eo) = wv;
;         s0 = d0 * s0 + u0; s1 = d1 * s1 + u1; }
	v_cvt_pk_bf16_f32 v28, v12, v13
	v_cvt_pk_bf16_f32 v29, v14, v15
	v_cvt_pk_bf16_f32 v30, v16, v17
	v_cvt_pk_bf16_f32 v31, v18, v19
	global_store_dwordx4 v[6:7], v[28:31], off
	v_lshl_add_u64 v[6:7], v[6:7], 0, s[4:5]
	v_lshlrev_b32_e32 v20, 16, v226
	v_and_b32_e32 v21, 0xffff0000, v226
	v_lshlrev_b32_e32 v22, 16, v227
	v_and_b32_e32 v23, 0xffff0000, v227
	v_lshlrev_b32_e32 v24, 16, v228
	v_and_b32_e32 v25, 0xffff0000, v228
	v_lshlrev_b32_e32 v26, 16, v229
	v_and_b32_e32 v27, 0xffff0000, v229
	v_pk_fma_f32 v[12:13], v[12:13], v[230:231], v[20:21]
	v_pk_fma_f32 v[14:15], v[14:15], v[232:233], v[22:23]
	v_pk_fma_f32 v[16:17], v[16:17], v[234:235], v[24:25]
	v_pk_fma_f32 v[18:19], v[18:19], v[236:237], v[26:27]
	global_load_dwordx4 v[226:229], v[4:5], off
	v_lshl_add_u64 v[4:5], v[4:5], 0, s[4:5]
	global_load_dwordx4 v[230:233], v[10:11], off offset:1536
	global_load_dwordx4 v[234:237], v[10:11], off offset:1552
	s_waitcnt vmcnt(36)
	v_cvt_pk_bf16_f32 v28, v12, v13
	v_cvt_pk_bf16_f32 v29, v14, v15
	v_cvt_pk_bf16_f32 v30, v16, v17
	v_cvt_pk_bf16_f32 v31, v18, v19
	global_store_dwordx4 v[6:7], v[28:31], off
	v_lshl_add_u64 v[6:7], v[6:7], 0, s[4:5]
	v_lshlrev_b32_e32 v20, 16, v118
	v_and_b32_e32 v21, 0xffff0000, v118
	v_lshlrev_b32_e32 v22, 16, v119
	v_and_b32_e32 v23, 0xffff0000, v119
	v_lshlrev_b32_e32 v24, 16, v120
	v_and_b32_e32 v25, 0xffff0000, v120
	v_lshlrev_b32_e32 v26, 16, v121
	v_and_b32_e32 v27, 0xffff0000, v121
	v_pk_fma_f32 v[12:13], v[12:13], v[122:123], v[20:21]
	v_pk_fma_f32 v[14:15], v[14:15], v[124:125], v[22:23]
	v_pk_fma_f32 v[16:17], v[16:17], v[126:127], v[24:25]
	v_pk_fma_f32 v[18:19], v[18:19], v[128:129], v[26:27]
	global_load_dwordx4 v[118:121], v[4:5], off
	v_lshl_add_u64 v[4:5], v[4:5], 0, s[4:5]
	global_load_dwordx4 v[122:125], v[10:11], off offset:2048
	global_load_dwordx4 v[126:129], v[10:11], off offset:2064
	s_waitcnt vmcnt(36)
	v_cvt_pk_bf16_f32 v28, v12, v13
	v_cvt_pk_bf16_f32 v29, v14, v15
	v_cvt_pk_bf16_f32 v30, v16, v17
	v_cvt_pk_bf16_f32 v31, v18, v19
	global_store_dwordx4 v[6:7], v[28:31], off
	v_lshl_add_u64 v[6:7], v[6:7], 0, s[4:5]
	v_lshlrev_b32_e32 v20, 16, v130
	v_and_b32_e32 v21, 0xffff0000, v130
	v_lshlrev_b32_e32 v22, 16, v131
	v_and_b32_e32 v23, 0xffff0000, v131
	v_lshlrev_b32_e32 v24, 16, v132
	v_and_b32_e32 v25, 0xffff0000, v132
	v_lshlrev_b32_e32 v26, 16, v133
	v_and_b32_e32 v27, 0xffff0000, v133
	v_pk_fma_f32 v[12:13], v[12:13], v[134:135], v[20:21]
	v_pk_fma_f32 v[14:15], v[14:15], v[136:137], v[22:23]
	v_pk_fma_f32 v[16:17], v[16:17], v[138:139], v[24:25]
	v_pk_fma_f32 v[18:19], v[18:19], v[140:141], v[26:27]
	global_load_dwordx4 v[130:133], v[4:5], off
	v_lshl_add_u64 v[4:5], v[4:5], 0, s[4:5]
	global_load_dwordx4 v[134:137], v[10:11], off offset:2560
	global_load_dwordx4 v[138:141], v[10:11], off offset:2576
	s_waitcnt vmcnt(36)
	v_cvt_pk_bf16_f32 v28, v12, v13
	v_cvt_pk_bf16_f32 v29, v14, v15
	v_cvt_pk_bf16_f32 v30, v16, v17
	v_cvt_pk_bf16_f32 v31, v18, v19
	global_store_dwordx4 v[6:7], v[28:31], off
	v_lshl_add_u64 v[6:7], v[6:7], 0, s[4:5]
	v_lshlrev_b32_e32 v20, 16, v142
	v_and_b32_e32 v21, 0xffff0000, v142
	v_lshlrev_b32_e32 v22, 16, v143
	v_and_b32_e32 v23, 0xffff0000, v143
	v_lshlrev_b32_e32 v24, 16, v144
	v_and_b32_e32 v25, 0xffff0000, v144
	v_lshlrev_b32_e32 v26, 16, v145
	v_and_b32_e32 v27, 0xffff0000, v145
	v_pk_fma_f32 v[12:13], v[12:13], v[146:147], v[20:21]
	v_pk_fma_f32 v[14:15], v[14:15], v[148:149], v[22:23]
	v_pk_fma_f32 v[16:17], v[16:17], v[150:151], v[24:25]
	v_pk_fma_f32 v[18:19], v[18:19], v[152:153], v[26:27]
	global_load_dwordx4 v[142:145], v[4:5], off
	v_lshl_add_u64 v[4:5], v[4:5], 0, s[4:5]
	global_load_dwordx4 v[146:149], v[10:11], off offset:3072
	global_load_dwordx4 v[150:153], v[10:11], off offset:3088
	s_waitcnt vmcnt(36)
	v_cvt_pk_bf16_f32 v28, v12, v13
	v_cvt_pk_bf16_f32 v29, v14, v15
	v_cvt_pk_bf16_f32 v30, v16, v17
	v_cvt_pk_bf16_f32 v31, v18, v19
	global_store_dwordx4 v[6:7], v[28:31], off
	v_lshl_add_u64 v[6:7], v[6:7], 0, s[4:5]
	v_lshlrev_b32_e32 v20, 16, v154
	v_and_b32_e32 v21, 0xffff0000, v154
	v_lshlrev_b32_e32 v22, 16, v155
	v_and_b32_e32 v23, 0xffff0000, v155
	v_lshlrev_b32_e32 v24, 16, v156
	v_and_b32_e32 v25, 0xffff0000, v156
	v_lshlrev_b32_e32 v26, 16, v157
	v_and_b32_e32 v27, 0xffff0000, v157
	v_pk_fma_f32 v[12:13], v[12:13], v[158:159], v[20:21]
	v_pk_fma_f32 v[14:15], v[14:15], v[160:161], v[22:23]
	v_pk_fma_f32 v[16:17], v[16:17], v[162:163], v[24:25]
	v_pk_fma_f32 v[18:19], v[18:19], v[164:165], v[26:27]
	global_load_dwordx4 v[154:157], v[4:5], off
	v_lshl_add_u64 v[4:5], v[4:5], 0, s[4:5]
	global_load_dwordx4 v[158:161], v[10:11], off offset:3584
	global_load_dwordx4 v[162:165], v[10:11], off offset:3600
	v_lshl_add_u64 v[10:11], v[10:11], 0, s[86:87]
	s_waitcnt vmcnt(36)
	v_cvt_pk_bf16_f32 v28, v12, v13
	v_cvt_pk_bf16_f32 v29, v14, v15
	v_cvt_pk_bf16_f32 v30, v16, v17
	v_cvt_pk_bf16_f32 v31, v18, v19
	global_store_dwordx4 v[6:7], v[28:31], off
	v_lshl_add_u64 v[6:7], v[6:7], 0, s[4:5]
	v_lshlrev_b32_e32 v20, 16, v166
	v_and_b32_e32 v21, 0xffff0000, v166
	v_lshlrev_b32_e32 v22, 16, v167
	v_and_b32_e32 v23, 0xffff0000, v167
	v_lshlrev_b32_e32 v24, 16, v168
	v_and_b32_e32 v25, 0xffff0000, v168
	v_lshlrev_b32_e32 v26, 16, v169
	v_and_b32_e32 v27, 0xffff0000, v169
	v_pk_fma_f32 v[12:13], v[12:13], v[170:171], v[20:21]
	v_pk_fma_f32 v[14:15], v[14:15], v[172:173], v[22:23]
	v_pk_fma_f32 v[16:17], v[16:17], v[174:175], v[24:25]
	v_pk_fma_f32 v[18:19], v[18:19], v[176:177], v[26:27]
	global_load_dwordx4 v[166:169], v[4:5], off
	v_lshl_add_u64 v[4:5], v[4:5], 0, s[4:5]
	global_load_dwordx4 v[170:173], v[10:11], off offset:0
	global_load_dwordx4 v[174:177], v[10:11], off offset:16
	s_waitcnt vmcnt(36)
; #define GAS __attribute__((address_space(1)))
; __device__ __forceinline__ unsigned cvt_pk_bf16(float lo, float hi) { unsigned r; asm volatile("v_cvt_pk_bf16_f32 %0, %1, %2" : "=v"(r) : "v"(lo), "v"(hi)); return r; }
; __device__ __forceinline__ void scan_item(Frame& F, int item) {
;     ...
; #pragma unroll 16
;     for (int n = 0; n < 32; ++n) { const size_t chunk = (size_t)bh * 32 + n; const size_t eo = chunk * 16384 + (size_t)vv * 128 + kk0;
;         const u32x4 ub = *(const GAS u32x4*)((const GAS bf16_t*)UT + eo); const f32x4 u0 = {bflo(ub.x), bfhi(ub.x), bflo(ub.y), bfhi(ub.y)}, u1 = {bflo(ub.z), bfhi(ub.z), bflo(ub.w), bfhi(ub.w)}, d0 = *(const GAS f32x4*)(DEC + chunk * 128 + kk0), d1 = *(const GAS f32x4*)(DEC + chunk * 128 + kk0 + 4);
;         u32x4 wv; wv.x = cvt_pk_bf16(s0[0], s0[1]); wv.y = cvt_pk_bf16(s0[2], s0[3]); wv.z = cvt_pk_bf16(s1[0], s1[1]); wv.w = cvt_pk_bf16(s1[2], s1[3]);
;         *(GAS u32x4*)(SPT + eo) = wv;
;         s0 = d0 * s0 + u0; s1 = d1 * s1 + u1; }
	v_cvt_pk_bf16_f32 v28, v12, v13
	v_cvt_pk_bf16_f32 v29, v14, v15
	v_cvt_pk_bf16_f32 v30, v16, v17
	v_cvt_pk_bf16_f32 v31, v18, v19
	global_store_dwordx4 v[6:7], v[28:31], off
	v_lshl_add_u64 v[6:7], v[6:7], 0, s[4:5]
	v_lshlrev_b32_e32 v20, 16, v178
	v_and_b32_e32 v21, 0xffff0000, v178
	v_lshlrev_b32_e32 v22, 16, v179
	v_and_b32_e32 v23, 0xffff0000, v179
	v_lshlrev_b32_e32 v24, 16, v180
	v_and_b32_e32 v25, 0xffff0000, v180
	v_lshlrev_b32_e32 v26, 16, v181
	v_and_b32_e32 v27, 0xffff0000, v181
	v_pk_fma_f32 v[12:13], v[12:13], v[182:183], v[20:21]
	v_pk_fma_f32 v[14:15], v[14:15], v[184:185], v[22:23]
	v_pk_fma_f32 v[16:17], v[16:17], v[186:187], v[24:25]
	v_pk_fma_f32 v[18:19], v[18:19], v[188:189], v[26:27]
	global_load_dwordx4 v[178:181], v[4:5], off
	v_lshl_add_u64 v[4:5], v[4:5], 0, s[4:5]
	global_load_dwordx4 v[182:185], v[10:11], off offset:512
	global_load_dwordx4 v[186:189], v[10:11], off offset:528
	s_waitcnt vmcnt(36)
	v_cvt_pk_bf16_f32 v28, v12, v13
	v_cvt_pk_bf16_f32 v29, v14, v15
	v_cvt_pk_bf16_f32 v30, v16, v17
	v_cvt_pk_bf16_f32 v31, v18, v19
	global_store_dwordx4 v[6:7], v[28:31], off
	v_lshl_add_u64 v[6:7], v[6:7], 0, s[4:5]
	v_lshlrev_b32_e32 v20, 16, v190
	v_and_b32_e32 v21, 0xffff0000, v190
	v_lshlrev_b32_e32 v22, 16, v191
	v_and_b32_e32 v23, 0xffff0000, v191
	v_lshlrev_b32_e32 v24, 16, v192
	v_and_b32_e32 v25, 0xffff0000, v192
	v_lshlrev_b32_e32 v26, 16, v193
	v_and_b32_e32 v27, 0xffff0000, v193
	v_pk_fma_f32 v[12:13], v[12:13], v[194:195], v[20:21]
	v_pk_fma_f32 v[14:15], v[14:15], v[196:197], v[22:23]
	v_pk_fma_f32 v[16:17], v[16:17], v[198:199], v[24:25]
	v_pk_fma_f32 v[18:19], v[18:19], v[200:201], v[26:27]
	global_load_dwordx4 v[190:193], v[4:5], off
	v_lshl_add_u64 v[4:5], v[4:5], 0, s[4:5]
	global_load_dwordx4 v[194:197], v[10:11], off offset:1024
	global_load_dwordx4 v[198:201], v[10:11], off offset:1040
	s_waitcnt vmcnt(36)
	v_cvt_pk_bf16_f32 v28, v12, v13
	v_cvt_pk_bf16_f32 v29, v14, v15
	v_cvt_pk_bf16_f32 v30, v16, v17
	v_cvt_pk_bf16_f32 v31, v18, v19
	global_store_dwordx4 v[6:7], v[28:31], off
	v_lshl_add_u64 v[6:7], v[6:7], 0, s[4:5]
	v_lshlrev_b32_e32 v20, 16, v202
	v_and_b32_e32 v21, 0xffff0000, v202
	v_lshlrev_b32_e32 v22, 16, v203
	v_and_b32_e32 v23, 0xffff0000, v203
	v_lshlrev_b32_e32 v24, 16, v204
	v_and_b32_e32 v25, 0xffff0000, v204
	v_lshlrev_b32_e32 v26, 16, v205
	v_and_b32_e32 v27, 0xffff0000, v205
	v_pk_fma_f32 v[12:13], v[12:13], v[206:207], v[20:21]
	v_pk_fma_f32 v[14:15], v[14:15], v[208:209], v[22:23]
	v_pk_fma_f32 v[16:17], v[16:17], v[210:211], v[24:25]
	v_pk_fma_f32 v[18:19], v[18:19], v[212:213], v[26:27]
	global_load_dwordx4 v[202:205], v[4:5], off
	v_lshl_add_u64 v[4:5], v[4:5], 0, s[4:5]
	global_load_dwordx4 v[206:209], v[10:11], off offset:1536
	global_load_dwordx4 v[210:213], v[10:11], off offset:1552
	s_waitcnt vmcnt(36)
	v_cvt_pk_bf16_f32 v28, v12, v13
	v_cvt_pk_bf16_f32 v29, v14, v15
	v_cvt_pk_bf16_f32 v30, v16, v17
	v_cvt_pk_bf16_f32 v31, v18, v19
	global_store_dwordx4 v[6:7], v[28:31], off
	v_lshl_add_u64 v[6:7], v[6:7], 0, s[4:5]
	v_lshlrev_b32_e32 v20, 16, v214
	v_and_b32_e32 v21, 0xffff0000, v214
	v_lshlrev_b32_e32 v22, 16, v215
	v_and_b32_e32 v23, 0xffff0000, v215
	v_lshlrev_b32_e32 v24, 16, v216
	v_and_b32_e32 v25, 0xffff0000, v216
	v_lshlrev_b32_e32 v26, 16, v217
	v_and_b32_e32 v27, 0xffff0000, v217
	v_pk_fma_f32 v[12:13], v[12:13], v[218:219], v[20:21]
	v_pk_fma_f32 v[14:15], v[14:15], v[220:221], v[22:23]
	v_pk_fma_f32 v[16:17], v[16:17], v[222:223], v[24:25]
	v_pk_fma_f32 v[18:19], v[18:19], v[224:225], v[26:27]
	global_load_dwordx4 v[214:217], v[4:5], off
	v_lshl_add_u64 v[4:5], v[4:5], 0, s[4:5]
	global_load_dwordx4 v[218:221], v[10:11], off offset:2048
	global_load_dwordx4 v[222:225], v[10:11], off offset:2064
	s_waitcnt vmcnt(36)
	v_cvt_pk_bf16_f32 v28, v12, v13
	v_cvt_pk_bf16_f32 v29, v14, v15
	v_cvt_pk_bf16_f32 v30, v16, v17
	v_cvt_pk_bf16_f32 v31, v18, v19
	global_store_dwordx4 v[6:7], v[28:31], off
	v_lshl_add_u64 v[6:7], v[6:7], 0, s[4:5]
	v_lshlrev_b32_e32 v20, 16, v226
	v_and_b32_e32 v21, 0xffff0000, v226
	v_lshlrev_b32_e32 v22, 16, v227
	v_and_b32_e32 v23, 0xffff0000, v227
	v_lshlrev_b32_e32 v24, 16, v228
	v_and_b32_e32 v25, 0xffff0000, v228
	v_lshlrev_b32_e32 v26, 16, v229
	v_and_b32_e32 v27, 0xffff0000, v229
	v_pk_fma_f32 v[12:13], v[12:13], v[230:231], v[20:21]
	v_pk_fma_f32 v[14:15], v[14:15], v[232:233], v[22:23]
	v_pk_fma_f32 v[16:17], v[16:17], v[234:235], v[24:25]
	v_pk_fma_f32 v[18:19], v[18:19], v[236:237], v[26:27]
	global_load_dwordx4 v[226:229], v[4:5], off
	v_lshl_add_u64 v[4:5], v[4:5], 0, s[4:5]
	global_load_dwordx4 v[230:233], v[10:11], off offset:2560
	global_load_dwordx4 v[234:237], v[10:11], off offset:2576
	s_waitcnt vmcnt(36)
	v_cvt_pk_bf16_f32 v28, v12, v13
	v_cvt_pk_bf16_f32 v29, v14, v15
	v_cvt_pk_bf16_f32 v30, v16, v17
	v_cvt_pk_bf16_f32 v31, v18, v19
	global_store_dwordx4 v[6:7], v[28:31], off
	v_lshl_add_u64 v[6:7], v[6:7], 0, s[4:5]
	v_lshlrev_b32_e32 v20, 16, v118
	v_and_b32_e32 v21, 0xffff0000, v118
	v_lshlrev_b32_e32 v22, 16, v119
	v_and_b32_e32 v23, 0xffff0000, v119
	v_lshlrev_b32_e32 v24, 16, v120
	v_and_b32_e32 v25, 0xffff0000, v120
	v_lshlrev_b32_e32 v26, 16, v121
	v_and_b32_e32 v27, 0xffff0000, v121
	v_pk_fma_f32 v[12:13], v[12:13], v[122:123], v[20:21]
	v_pk_fma_f32 v[14:15], v[14:15], v[124:125], v[22:23]
	v_pk_fma_f32 v[16:17], v[16:17], v[126:127], v[24:25]
	v_pk_fma_f32 v[18:19], v[18:19], v[128:129], v[26:27]
	global_load_dwordx4 v[118:121], v[4:5], off
	v_lshl_add_u64 v[4:5], v[4:5], 0, s[4:5]
	global_load_dwordx4 v[122:125], v[10:11], off offset:3072
	global_load_dwordx4 v[126:129], v[10:11], off offset:3088
	s_waitcnt vmcnt(36)
; #define GAS __attribute__((address_space(1)))
; __device__ __forceinline__ unsigned cvt_pk_bf16(float lo, float hi) { unsigned r; asm volatile("v_cvt_pk_bf16_f32 %0, %1, %2" : "=v"(r) : "v"(lo), "v"(hi)); return r; }
; __device__ __forceinline__ void scan_item(Frame& F, int item) {
;     ...
; #pragma unroll 16
;     for (int n = 0; n < 32; ++n) { const size_t chunk = (size_t)bh * 32 + n; const size_t eo = chunk * 16384 + (size_t)vv * 128 + kk0;
;         const u32x4 ub = *(const GAS u32x4*)((const GAS bf16_t*)UT + eo); const f32x4 u0 = {bflo(ub.x), bfhi(ub.x), bflo(ub.y), bfhi(ub.y)}, u1 = {bflo(ub.z), bfhi(ub.z), bflo(ub.w), bfhi(ub.w)}, d0 = *(const GAS f32x4*)(DEC + chunk * 128 + kk0), d1 = *(const GAS f32x4*)(DEC + chunk * 128 + kk0 + 4);
;         u32x4 wv; wv.x = cvt_pk_bf16(s0[0], s0[1]); wv.y = cvt_pk_bf16(s0[2], s0[3]); wv.z = cvt_pk_bf16(s1[0], s1[1]); wv.w = cvt_pk_bf16(s1[2], s1[3]);
;         *(GAS u32x4*)(SPT + eo) = wv;
;         s0 = d0 * s0 + u0; s1 = d1 * s1 + u1; }
	v_cvt_pk_bf16_f32 v28, v12, v13
	v_cvt_pk_bf16_f32 v29, v14, v15
	v_cvt_pk_bf16_f32 v30, v16, v17
	v_cvt_pk_bf16_f32 v31, v18, v19
	global_store_dwordx4 v[6:7], v[28:31], off
	v_lshl_add_u64 v[6:7], v[6:7], 0, s[4:5]
	v_lshlrev_b32_e32 v20, 16, v130
	v_and_b32_e32 v21, 0xffff0000, v130
	v_lshlrev_b32_e32 v22, 16, v131
	v_and_b32_e32 v23, 0xffff0000, v131
	v_lshlrev_b32_e32 v24, 16, v132
	v_and_b32_e32 v25, 0xffff0000, v132
	v_lshlrev_b32_e32 v26, 16, v133
	v_and_b32_e32 v27, 0xffff0000, v133
	v_pk_fma_f32 v[12:13], v[12:13], v[134:135], v[20:21]
	v_pk_fma_f32 v[14:15], v[14:15], v[136:137], v[22:23]
	v_pk_fma_f32 v[16:17], v[16:17], v[138:139], v[24:25]
	v_pk_fma_f32 v[18:19], v[18:19], v[140:141], v[26:27]
	global_load_dwordx4 v[130:133], v[4:5], off
	v_lshl_add_u64 v[4:5], v[4:5], 0, s[4:5]
	global_load_dwordx4 v[134:137], v[10:11], off offset:3584
	global_load_dwordx4 v[138:141], v[10:11], off offset:3600
	v_lshl_add_u64 v[10:11], v[10:11], 0, s[86:87]
	s_waitcnt vmcnt(36)
	v_cvt_pk_bf16_f32 v28, v12, v13
	v_cvt_pk_bf16_f32 v29, v14, v15
	v_cvt_pk_bf16_f32 v30, v16, v17
	v_cvt_pk_bf16_f32 v31, v18, v19
	global_store_dwordx4 v[6:7], v[28:31], off
	v_lshl_add_u64 v[6:7], v[6:7], 0, s[4:5]
	v_lshlrev_b32_e32 v20, 16, v142
	v_and_b32_e32 v21, 0xffff0000, v142
	v_lshlrev_b32_e32 v22, 16, v143
	v_and_b32_e32 v23, 0xffff0000, v143
	v_lshlrev_b32_e32 v24, 16, v144
	v_and_b32_e32 v25, 0xffff0000, v144
	v_lshlrev_b32_e32 v26, 16, v145
	v_and_b32_e32 v27, 0xffff0000, v145
	v_pk_fma_f32 v[12:13], v[12:13], v[146:147], v[20:21]
	v_pk_fma_f32 v[14:15], v[14:15], v[148:149], v[22:23]
	v_pk_fma_f32 v[16:17], v[16:17], v[150:151], v[24:25]
	v_pk_fma_f32 v[18:19], v[18:19], v[152:153], v[26:27]
	s_waitcnt vmcnt(33)
	v_cvt_pk_bf16_f32 v28, v12, v13
	v_cvt_pk_bf16_f32 v29, v14, v15
	v_cvt_pk_bf16_f32 v30, v16, v17
	v_cvt_pk_bf16_f32 v31, v18, v19
	global_store_dwordx4 v[6:7], v[28:31], off
	v_lshl_add_u64 v[6:7], v[6:7], 0, s[4:5]
	v_lshlrev_b32_e32 v20, 16, v154
	v_and_b32_e32 v21, 0xffff0000, v154
	v_lshlrev_b32_e32 v22, 16, v155
	v_and_b32_e32 v23, 0xffff0000, v155
	v_lshlrev_b32_e32 v24, 16, v156
	v_and_b32_e32 v25, 0xffff0000, v156
	v_lshlrev_b32_e32 v26, 16, v157
	v_and_b32_e32 v27, 0xffff0000, v157
	v_pk_fma_f32 v[12:13], v[12:13], v[158:159], v[20:21]
	v_pk_fma_f32 v[14:15], v[14:15], v[160:161], v[22:23]
	v_pk_fma_f32 v[16:17], v[16:17], v[162:163], v[24:25]
	v_pk_fma_f32 v[18:19], v[18:19], v[164:165], v[26:27]
	s_waitcnt vmcnt(30)
	v_cvt_pk_bf16_f32 v28, v12, v13
	v_cvt_pk_bf16_f32 v29, v14, v15
	v_cvt_pk_bf16_f32 v30, v16, v17
	v_cvt_pk_bf16_f32 v31, v18, v19
	global_store_dwordx4 v[6:7], v[28:31], off
	v_lshl_add_u64 v[6:7], v[6:7], 0, s[4:5]
	v_lshlrev_b32_e32 v20, 16, v166
	v_and_b32_e32 v21, 0xffff0000, v166
	v_lshlrev_b32_e32 v22, 16, v167
	v_and_b32_e32 v23, 0xffff0000, v167
	v_lshlrev_b32_e32 v24, 16, v168
	v_and_b32_e32 v25, 0xffff0000, v168
	v_lshlrev_b32_e32 v26, 16, v169
	v_and_b32_e32 v27, 0xffff0000, v169
	v_pk_fma_f32 v[12:13], v[12:13], v[170:171], v[20:21]
	v_pk_fma_f32 v[14:15], v[14:15], v[172:173], v[22:23]
	v_pk_fma_f32 v[16:17], v[16:17], v[174:175], v[24:25]
	v_pk_fma_f32 v[18:19], v[18:19], v[176:177], v[26:27]
	s_waitcnt vmcnt(27)
	v_cvt_pk_bf16_f32 v28, v12, v13
	v_cvt_pk_bf16_f32 v29, v14, v15
	v_cvt_pk_bf16_f32 v30, v16, v17
	v_cvt_pk_bf16_f32 v31, v18, v19
	global_store_dwordx4 v[6:7], v[28:31], off
	v_lshl_add_u64 v[6:7], v[6:7], 0, s[4:5]
	v_lshlrev_b32_e32 v20, 16, v178
	v_and_b32_e32 v21, 0xffff0000, v178
	v_lshlrev_b32_e32 v22, 16, v179
	v_and_b32_e32 v23, 0xffff0000, v179
	v_lshlrev_b32_e32 v24, 16, v180
	v_and_b32_e32 v25, 0xffff0000, v180
	v_lshlrev_b32_e32 v26, 16, v181
	v_and_b32_e32 v27, 0xffff0000, v181
	v_pk_fma_f32 v[12:13], v[12:13], v[182:183], v[20:21]
	v_pk_fma_f32 v[14:15], v[14:15], v[184:185], v[22:23]
	v_pk_fma_f32 v[16:17], v[16:17], v[186:187], v[24:25]
	v_pk_fma_f32 v[18:19], v[18:19], v[188:189], v[26:27]
	s_waitcnt vmcnt(24)
; #define GAS __attribute__((address_space(1)))
; __device__ __forceinline__ unsigned cvt_pk_bf16(float lo, float hi) { unsigned r; asm volatile("v_cvt_pk_bf16_f32 %0, %1, %2" : "=v"(r) : "v"(lo), "v"(hi)); return r; }
; __device__ __forceinline__ void scan_item(Frame& F, int item) {
;     ...
; #pragma unroll 16
;     for (int n = 0; n < 32; ++n) { const size_t chunk = (size_t)bh * 32 + n; const size_t eo = chunk * 16384 + (size_t)vv * 128 + kk0;
;         const u32x4 ub = *(const GAS u32x4*)((const GAS bf16_t*)UT + eo); const f32x4 u0 = {bflo(ub.x), bfhi(ub.x), bflo(ub.y), bfhi(ub.y)}, u1 = {bflo(ub.z), bfhi(ub.z), bflo(ub.w), bfhi(ub.w)}, d0 = *(const GAS f32x4*)(DEC + chunk * 128 + kk0), d1 = *(const GAS f32x4*)(DEC + chunk * 128 + kk0 + 4);
;         u32x4 wv; wv.x = cvt_pk_bf16(s0[0], s0[1]); wv.y = cvt_pk_bf16(s0[2], s0[3]); wv.z = cvt_pk_bf16(s1[0], s1[1]); wv.w = cvt_pk_bf16(s1[2], s1[3]);
;         *(GAS u32x4*)(SPT + eo) = wv;
;         s0 = d0 * s0 + u0; s1 = d1 * s1 + u1; }
	v_cvt_pk_bf16_f32 v28, v12, v13
	v_cvt_pk_bf16_f32 v29, v14, v15
	v_cvt_pk_bf16_f32 v30, v16, v17
	v_cvt_pk_bf16_f32 v31, v18, v19
	global_store_dwordx4 v[6:7], v[28:31], off
	v_lshl_add_u64 v[6:7], v[6:7], 0, s[4:5]
	v_lshlrev_b32_e32 v20, 16, v190
	v_and_b32_e32 v21, 0xffff0000, v190
	v_lshlrev_b32_e32 v22, 16, v191
	v_and_b32_e32 v23, 0xffff0000, v191
	v_lshlrev_b32_e32 v24, 16, v192
	v_and_b32_e32 v25, 0xffff0000, v192
	v_lshlrev_b32_e32 v26, 16, v193
	v_and_b32_e32 v27, 0xffff0000, v193
	v_pk_fma_f32 v[12:13], v[12:13], v[194:195], v[20:21]
	v_pk_fma_f32 v[14:15], v[14:15], v[196:197], v[22:23]
	v_pk_fma_f32 v[16:17], v[16:17], v[198:199], v[24:25]
	v_pk_fma_f32 v[18:19], v[18:19], v[200:201], v[26:27]
	s_waitcnt vmcnt(21)
	v_cvt_pk_bf16_f32 v28, v12, v13
	v_cvt_pk_bf16_f32 v29, v14, v15
	v_cvt_pk_bf16_f32 v30, v16, v17
	v_cvt_pk_bf16_f32 v31, v18, v19
	global_store_dwordx4 v[6:7], v[28:31], off
	v_lshl_add_u64 v[6:7], v[6:7], 0, s[4:5]
	v_lshlrev_b32_e32 v20, 16, v202
	v_and_b32_e32 v21, 0xffff0000, v202
	v_lshlrev_b32_e32 v22, 16, v203
	v_and_b32_e32 v23, 0xffff0000, v203
	v_lshlrev_b32_e32 v24, 16, v204
	v_and_b32_e32 v25, 0xffff0000, v204
	v_lshlrev_b32_e32 v26, 16, v205
	v_and_b32_e32 v27, 0xffff0000, v205
	v_pk_fma_f32 v[12:13], v[12:13], v[206:207], v[20:21]
	v_pk_fma_f32 v[14:15], v[14:15], v[208:209], v[22:23]
	v_pk_fma_f32 v[16:17], v[16:17], v[210:211], v[24:25]
	v_pk_fma_f32 v[18:19], v[18:19], v[212:213], v[26:27]
	s_waitcnt vmcnt(18)
	v_cvt_pk_bf16_f32 v28, v12, v13
	v_cvt_pk_bf16_f32 v29, v14, v15
	v_cvt_pk_bf16_f32 v30, v16, v17
	v_cvt_pk_bf16_f32 v31, v18, v19
	global_store_dwordx4 v[6:7], v[28:31], off
	v_lshl_add_u64 v[6:7], v[6:7], 0, s[4:5]
	v_lshlrev_b32_e32 v20, 16, v214
	v_and_b32_e32 v21, 0xffff0000, v214
	v_lshlrev_b32_e32 v22, 16, v215
	v_and_b32_e32 v23, 0xffff0000, v215
	v_lshlrev_b32_e32 v24, 16, v216
	v_and_b32_e32 v25, 0xffff0000, v216
	v_lshlrev_b32_e32 v26, 16, v217
	v_and_b32_e32 v27, 0xffff0000, v217
	v_pk_fma_f32 v[12:13], v[12:13], v[218:219], v[20:21]
	v_pk_fma_f32 v[14:15], v[14:15], v[220:221], v[22:23]
	v_pk_fma_f32 v[16:17], v[16:17], v[222:223], v[24:25]
	v_pk_fma_f32 v[18:19], v[18:19], v[224:225], v[26:27]
	s_waitcnt vmcnt(15)
	v_cvt_pk_bf16_f32 v28, v12, v13
	v_cvt_pk_bf16_f32 v29, v14, v15
	v_cvt_pk_bf16_f32 v30, v16, v17
	v_cvt_pk_bf16_f32 v31, v18, v19
	global_store_dwordx4 v[6:7], v[28:31], off
	v_lshl_add_u64 v[6:7], v[6:7], 0, s[4:5]
	v_lshlrev_b32_e32 v20, 16, v226
	v_and_b32_e32 v21, 0xffff0000, v226
	v_lshlrev_b32_e32 v22, 16, v227
	v_and_b32_e32 v23, 0xffff0000, v227
	v_lshlrev_b32_e32 v24, 16, v228
	v_and_b32_e32 v25, 0xffff0000, v228
	v_lshlrev_b32_e32 v26, 16, v229
	v_and_b32_e32 v27, 0xffff0000, v229
	v_pk_fma_f32 v[12:13], v[12:13], v[230:231], v[20:21]
	v_pk_fma_f32 v[14:15], v[14:15], v[232:233], v[22:23]
	v_pk_fma_f32 v[16:17], v[16:17], v[234:235], v[24:25]
	v_pk_fma_f32 v[18:19], v[18:19], v[236:237], v[26:27]
	s_waitcnt vmcnt(12)
	v_cvt_pk_bf16_f32 v28, v12, v13
	v_cvt_pk_bf16_f32 v29, v14, v15
	v_cvt_pk_bf16_f32 v30, v16, v17
	v_cvt_pk_bf16_f32 v31, v18, v19
	global_store_dwordx4 v[6:7], v[28:31], off
	v_lshl_add_u64 v[6:7], v[6:7], 0, s[4:5]
	v_lshlrev_b32_e32 v20, 16, v118
	v_and_b32_e32 v21, 0xffff0000, v118
	v_lshlrev_b32_e32 v22, 16, v119
	v_and_b32_e32 v23, 0xffff0000, v119
	v_lshlrev_b32_e32 v24, 16, v120
	v_and_b32_e32 v25, 0xffff0000, v120
	v_lshlrev_b32_e32 v26, 16, v121
	v_and_b32_e32 v27, 0xffff0000, v121
	v_pk_fma_f32 v[12:13], v[12:13], v[122:123], v[20:21]
	v_pk_fma_f32 v[14:15], v[14:15], v[124:125], v[22:23]
	v_pk_fma_f32 v[16:17], v[16:17], v[126:127], v[24:25]
	v_pk_fma_f32 v[18:19], v[18:19], v[128:129], v[26:27]
	s_waitcnt vmcnt(9)
	v_cvt_pk_bf16_f32 v28, v12, v13
	v_cvt_pk_bf16_f32 v29, v14, v15
	v_cvt_pk_bf16_f32 v30, v16, v17
	v_cvt_pk_bf16_f32 v31, v18, v19
	global_store_dwordx4 v[6:7], v[28:31], off
	v_lshl_add_u64 v[6:7], v[6:7], 0, s[4:5]
	v_lshlrev_b32_e32 v20, 16, v130
	v_and_b32_e32 v21, 0xffff0000, v130
	v_lshlrev_b32_e32 v22, 16, v131
	v_and_b32_e32 v23, 0xffff0000, v131
	v_lshlrev_b32_e32 v24, 16, v132
	v_and_b32_e32 v25, 0xffff0000, v132
	v_lshlrev_b32_e32 v26, 16, v133
	v_and_b32_e32 v27, 0xffff0000, v133
	v_pk_fma_f32 v[12:13], v[12:13], v[134:135], v[20:21]
	v_pk_fma_f32 v[14:15], v[14:15], v[136:137], v[22:23]
	v_pk_fma_f32 v[16:17], v[16:17], v[138:139], v[24:25]
	v_pk_fma_f32 v[18:19], v[18:19], v[140:141], v[26:27]
	s_add_i32 s85, s85, s0
	s_add_i32 s2, s2, s3
	s_cmpk_gt_i32 s85, 0xff
	s_cbranch_scc0 .LBB0_887
